# K2 tail: flag read merged with hist preloads after the barrier; epilogue address math hoisted before the barrier
# baseline (speedup 1.0000x reference)
.Lk2t_done:
	v_mov_b32_e32 v41, 0x18500
	v_or_b32_e32 v36, v165, v166
	v_or_b32_e32 v37, v158, v166
	v_or_b32_e32 v38, v150, v166
	v_or_b32_e32 v39, v146, v166
	v_lshl_or_b32 v40, v164, 4, v166
	v_add_u32_e32 v40, 0x140, v40
	v_lshl_add_u32 v36, v36, 2, v41
	v_lshl_add_u32 v37, v37, 2, v41
	v_lshl_add_u32 v38, v38, 2, v41
	v_lshl_add_u32 v39, v39, 2, v41
	v_lshl_add_u32 v40, v40, 2, v41
	v_mov_b32_e32 v22, 0x19440
	s_waitcnt lgkmcnt(0)
	s_barrier
	ds_read_b32 v22, v22
	ds_read_b32 v36, v36
	ds_read_b32 v37, v37
	ds_read_b32 v38, v38
	ds_read_b32 v39, v39
	ds_read_b32 v40, v40
	s_waitcnt lgkmcnt(5)
	v_cmp_ne_u32_e32 vcc, 0, v22
	s_cbranch_vccz .Lk2_epi_body
	v_or_b32_e32 v1, 0x80, v1
	s_mov_b64 s[0:1], 0
	v_mov_b32_e32 v24, 0x18b40
	v_mov_b32_e32 v23, 0
	v_mov_b32_e32 v25, 1
	s_movk_i32 s8, 0xfa
	v_mov_b32_e32 v26, 0x18fc0
	v_mov_b32_e32 v27, 0x18500
	v_mov_b32_e32 v28, v164
	s_branch .LBB1_158

.Lk2_epi_body:
	v_or_b32_e32 v23, v165, v166
	v_lshlrev_b32_e32 v0, 3, v167
	v_mov_b32_e32 v1, 0
	v_add_u32_e32 v22, s30, v23
	s_mov_b32 s2, 0x186a0
	v_lshl_add_u64 v[0:1], s[28:29], 0, v[0:1]
	v_cmp_gt_i32_e32 vcc, s2, v22
	s_and_saveexec_b64 s[0:1], vcc
	s_cbranch_execz .LBB1_169
	v_mov_b32_e32 v24, 0x18500
	v_lshl_add_u32 v23, v23, 2, v24
	s_waitcnt lgkmcnt(0)
	v_mov_b32_e32 v23, v36
	v_cvt_f32_u32_e32 v23, v23
	v_max_f32_e32 v23, 1.0, v23
	v_rsq_f32_e32 v24, v23
	v_lshlrev_b32_e32 v42, 2, v22
	s_mov_b64 s[6:7], exec
	v_cmp_eq_u32_e32 vcc, 0, v167
	s_and_b64 exec, exec, vcc
	global_store_dword v42, v24, s[24:25]
	s_mov_b64 exec, s[6:7]
	v_ashrrev_i32_e32 v23, 31, v22
	v_lshlrev_b64 v[22:23], 5, v[22:23]
	v_pk_mul_f32 v[2:3], v[2:3], v[24:25] op_sel_hi:[1,0]
	v_pk_mul_f32 v[4:5], v[4:5], v[24:25] op_sel_hi:[1,0]
	v_cvt_pk_bf16_f32 v2, v2, v3
	v_cvt_pk_bf16_f32 v3, v4, v5
	v_lshl_add_u64 v[4:5], v[0:1], 0, v[22:23]
	global_store_dwordx2 v[4:5], v[2:3], off
